# k_iter(non-first): slot-table loads issued before the NC scalar load returns, masks applied after
# baseline (speedup 1.0000x reference)
.LBB2_154:
	v_pk_add_f16 v21, v18, v1
	v_pk_add_f16 v36, v22, v2
	v_pk_add_f16 v37, v24, v3
	v_pk_add_f16 v38, v25, v4
	v_pk_add_f16 v39, v26, v5
	v_pk_add_f16 v40, v28, v6
	v_pk_add_f16 v41, v29, v7
	v_pk_add_f16 v42, v30, v8
	v_pk_add_f16 v43, v32, v9
	v_pk_add_f16 v115, v33, v10
	v_pk_add_f16 v131, v34, v11
	v_pk_add_f16 v132, v47, v12
	v_pk_add_f16 v133, v51, v13
	v_pk_add_f16 v134, v52, v14
	v_pk_add_f16 v135, v56, v15
	v_pk_add_f16 v136, v59, v16
	s_mov_b64 s[16:17], -1
	s_mov_b64 s[22:23], 0
	s_and_b64 vcc, exec, s[16:17]
	s_mov_b64 s[16:17], 0
	s_cbranch_vccz .LBB2_68
	s_branch .LBB2_67
	.p2align	8

_Z6k_iterILb0ELb0EEvPKfS1_PKiPK15HIP_vector_typeIfLj4EES7_S1_S1_S3_S1_PfS8_S1_S3_PDF16_PS5_SA_PiSA_SB_:
	s_load_dwordx2 s[8:9], s[0:1], 0x80
	s_load_dwordx4 s[4:7], s[0:1], 0x70
	s_load_dwordx4 s[16:19], s[0:1], 0x40
	v_readfirstlane_b32 s12, v0
	v_cmp_gt_u32_e64 s[14:15], 64, v0
	v_lshlrev_b32_e32 v1, 2, v0
	s_and_saveexec_b64 s[10:11], s[14:15]
	v_mov_b32_e32 v2, 0
	ds_write_b32 v1, v2 offset:5152
	s_or_b64 exec, exec, s[10:11]
	s_lshl_b32 s3, s2, 5
	s_and_b32 s3, s3, 0xe0
	s_lshr_b32 s2, s2, 3
	s_add_i32 s2, s3, s2
	s_lshl_b32 s25, s2, 6
	v_and_b32_e32 v2, 31, v0
	v_or_b32_e32 v4, s25, v2
	v_mov_b32_e32 v5, 0
	s_lshr_b32 s27, s12, 6
	s_lshl_b32 s32, s27, 2
	s_lshr_b32 s32, 0x73261540, s32
	s_lshl_b32 s32, s32, 5
	s_and_b32 s32, s32, 0xe0
	v_or_b32_e32 v176, s32, v2
	v_lshlrev_b32_e32 v177, 4, v176
	v_add_u32_e32 v178, 0x1000, v177
	v_add_u32_e32 v179, 0x2000, v177
	v_add_u32_e32 v180, 0x3000, v177
	v_add_u32_e32 v181, 0x4000, v177
	v_add_u32_e32 v182, 0x5000, v177
	s_mov_b32 s3, 0
	s_lshl_b64 s[34:35], s[2:3], 16
	s_lshl_b32 s33, s2, 2
	s_waitcnt lgkmcnt(0)
	s_load_dword s24, s[8:9], s33 offset:0x0
	s_add_u32 s20, s4, s34
	s_addc_u32 s21, s5, s35
	v_lshl_add_u64 v[4:5], v[4:5], 4, s[6:7]
	global_load_dwordx3 v[30:32], v[4:5], off
	global_load_dwordx3 v[26:28], v[4:5], off offset:512
	global_load_dwordx4 v[2:5], v177, s[20:21]
	global_load_dwordx4 v[6:9], v178, s[20:21]
	global_load_dwordx4 v[10:13], v179, s[20:21]
	global_load_dwordx4 v[14:17], v180, s[20:21]
	global_load_dwordx4 v[18:21], v181, s[20:21]
	global_load_dwordx4 v[22:25], v182, s[20:21]
	v_and_b32_e32 v38, 63, v0
	v_mov_b32_e32 v29, 0xff800000
	v_cmp_gt_u32_e64 s[0:1], 32, v38
	s_waitcnt lgkmcnt(0)
	s_cmpk_gt_i32 s24, 0x600
	s_cselect_b64 s[22:23], -1, 0
	s_cmpk_lt_i32 s24, 0x601
	s_cbranch_scc1 .LBB3_6
	s_and_saveexec_b64 s[8:9], s[14:15]
	s_cbranch_execz .LBB3_5
	v_or_b32_e32 v178, s25, v0
	v_mov_b32_e32 v179, 0
	v_lshl_add_u64 v[178:179], v[178:179], 4, s[6:7]
	global_load_dwordx4 v[178:181], v[178:179], off
	v_lshlrev_b32_e32 v177, 4, v0
	s_waitcnt vmcnt(0)
	ds_write_b128 v177, v[178:181] offset:2080
.LBB3_5:
	s_or_b64 exec, exec, s[8:9]
	s_waitcnt lgkmcnt(0)
	s_barrier
.LBB3_6:
	s_xor_b32 s33, s32, 0xff
	s_add_i32 s33, s33, s24
	s_ashr_i32 s26, s33, 8
	v_cmp_gt_i32_e32 vcc, s24, v176
	v_med3_i32 v33, s26, 0, 6
	s_sub_i32 s33, s24, 0x100
	v_cmp_gt_i32_e64 s[4:5], s33, v176
	s_sub_i32 s33, s24, 0x200
	v_cmp_gt_i32_e64 s[6:7], s33, v176
	s_sub_i32 s33, s24, 0x300
	v_cmp_gt_i32_e64 s[8:9], s33, v176
	s_sub_i32 s33, s24, 0x400
	v_cmp_gt_i32_e64 s[10:11], s33, v176
	s_sub_i32 s33, s24, 0x500
	v_cmp_gt_i32_e64 s[12:13], s33, v176
	s_and_b32 s25, s25, 0x7ffff000
	s_mov_b32 s2, 0xffff0000
	v_readfirstlane_b32 s26, v33
	s_nop 3
	s_cmp_lt_i32 s26, 4
	s_waitcnt vmcnt(5)
	v_cndmask_b32_e32 v4, v29, v4, vcc
	v_cndmask_b32_e64 v134, v3, v2, s[0:1]
	v_cndmask_b32_e32 v134, 0, v134, vcc
	s_waitcnt vmcnt(4)
	v_cndmask_b32_e64 v3, v29, v8, s[4:5]
	v_cndmask_b32_e64 v97, v7, v6, s[0:1]
	v_cndmask_b32_e64 v97, 0, v97, s[4:5]
	v_cndmask_b32_e64 v135, 1.0, v4, s[0:1]
	v_cndmask_b32_e64 v33, -1, v9, s[4:5]
	v_cndmask_b32_e64 v98, 1.0, v3, s[0:1]
	s_waitcnt vmcnt(3)
	v_cndmask_b32_e64 v6, v29, v12, s[6:7]
	v_cndmask_b32_e64 v68, v11, v10, s[0:1]
	v_cndmask_b32_e64 v68, 0, v68, s[6:7]
	s_waitcnt vmcnt(2)
	v_cndmask_b32_e64 v7, v29, v16, s[8:9]
	v_cndmask_b32_e64 v70, 1.0, v6, s[0:1]
	v_cndmask_b32_e64 v73, 1.0, v7, s[0:1]
	v_cndmask_b32_e64 v34, -1, v13, s[6:7]
	v_cndmask_b32_e64 v35, -1, v17, s[8:9]
	v_cndmask_b32_e64 v71, v15, v14, s[0:1]
	v_cndmask_b32_e64 v71, 0, v71, s[8:9]
	s_waitcnt vmcnt(1)
	v_cndmask_b32_e64 v8, v29, v20, s[10:11]
	v_cndmask_b32_e64 v48, 1.0, v8, s[0:1]
	s_waitcnt vmcnt(0)
	v_cndmask_b32_e64 v10, v29, v24, s[12:13]
	v_cndmask_b32_e32 v29, -1, v5, vcc
	v_max_i32_e32 v4, 0, v29
	v_add_u32_e32 v4, s25, v4
	v_mov_b32_e32 v5, 0
	v_lshl_add_u64 v[6:7], v[4:5], 2, s[16:17]
	v_max_i32_e32 v4, 0, v33
	v_add_u32_e32 v4, s25, v4
	v_lshl_add_u64 v[8:9], v[4:5], 2, s[16:17]
	v_max_i32_e32 v4, 0, v34
	v_add_u32_e32 v4, s25, v4
	v_cndmask_b32_e64 v3, 1.0, v10, s[0:1]
	v_lshl_add_u64 v[10:11], v[4:5], 2, s[16:17]
	v_max_i32_e32 v4, 0, v35
	v_cndmask_b32_e64 v36, -1, v21, s[10:11]
	v_add_u32_e32 v4, s25, v4
	v_lshl_add_u64 v[12:13], v[4:5], 2, s[16:17]
	v_max_i32_e32 v4, 0, v36
	v_cndmask_b32_e64 v37, -1, v25, s[12:13]
	v_add_u32_e32 v4, s25, v4
	v_lshl_add_u64 v[14:15], v[4:5], 2, s[16:17]
	v_max_i32_e32 v4, 0, v37
	v_cndmask_b32_e64 v46, v19, v18, s[0:1]
	v_cndmask_b32_e64 v46, 0, v46, s[10:11]
	v_cndmask_b32_e64 v2, v23, v22, s[0:1]
	v_cndmask_b32_e64 v2, 0, v2, s[12:13]
	v_add_u32_e32 v4, s25, v4
	v_lshl_add_u64 v[4:5], v[4:5], 2, s[16:17]
	global_load_dword v133, v[6:7], off
	global_load_dword v132, v[8:9], off
	global_load_dword v131, v[10:11], off
	global_load_dword v130, v[12:13], off
	global_load_dword v129, v[14:15], off
	global_load_dword v128, v[4:5], off
	v_max_f32_e32 v6, v32, v32
	v_cndmask_b32_e64 v4, v31, v30, s[0:1]
	v_max_f32_e32 v6, 0xc6ea6000, v6
	v_cndmask_b32_e64 v6, v6, 1.0, s[0:1]
	v_and_b32_e32 v7, 0xffff0000, v4
	v_sub_f32_e32 v8, v4, v7
	v_or_b32_sdwa v22, v4, v7 dst_sel:DWORD dst_unused:UNUSED_PAD src0_sel:WORD_1 src1_sel:DWORD
	v_and_b32_e32 v4, 0xffff0000, v6
	v_sub_f32_e32 v7, v6, v4
	v_or_b32_sdwa v24, v6, v4 dst_sel:DWORD dst_unused:UNUSED_PAD src0_sel:WORD_1 src1_sel:DWORD
	v_or_b32_sdwa v23, v8, v4 dst_sel:DWORD dst_unused:UNUSED_PAD src0_sel:WORD_1 src1_sel:DWORD
	v_max_f32_e32 v4, v28, v28
	v_cndmask_b32_e64 v5, v27, v26, s[0:1]
	v_and_b32_e32 v9, 0xffff0000, v7
	v_max_f32_e32 v4, 0xc6ea6000, v4
	v_sub_f32_e32 v9, v7, v9
	v_lshrrev_b32_e32 v7, 16, v7
	v_cndmask_b32_e64 v4, v4, 1.0, s[0:1]
	v_and_b32_e32 v6, 0xffff0000, v5
	v_and_or_b32 v25, v9, s2, v7
	v_sub_f32_e32 v7, v5, v6
	v_or_b32_sdwa v18, v5, v6 dst_sel:DWORD dst_unused:UNUSED_PAD src0_sel:WORD_1 src1_sel:DWORD
	v_and_b32_e32 v5, 0xffff0000, v4
	v_sub_f32_e32 v6, v4, v5
	v_and_b32_e32 v8, 0xffff0000, v6
	v_sub_f32_e32 v8, v6, v8
	v_lshrrev_b32_e32 v6, 16, v6
	v_or_b32_sdwa v20, v4, v5 dst_sel:DWORD dst_unused:UNUSED_PAD src0_sel:WORD_1 src1_sel:DWORD
	v_or_b32_sdwa v19, v7, v5 dst_sel:DWORD dst_unused:UNUSED_PAD src0_sel:WORD_1 src1_sel:DWORD
	v_and_or_b32 v21, v8, s2, v6
	s_mov_b64 s[2:3], 0
	s_cbranch_scc1 .LBB3_11
	s_cmp_gt_i32 s26, 4
	s_cbranch_scc0 .LBB3_14
	s_cmp_gt_i32 s26, 5
	s_cbranch_scc0 .LBB3_15
	s_cmp_eq_u32 s26, 6
	s_mov_b64 s[4:5], 0
	s_cbranch_scc0 .LBB3_48
	v_and_b32_e32 v4, 0xffff0000, v2
	v_max_f32_e32 v3, v3, v3
	v_sub_f32_e32 v4, v2, v4
	v_max_f32_e32 v3, 0xc6ea6000, v3
	v_and_b32_e32 v5, 0xffff0000, v3
	v_and_b32_e32 v4, 0xffff0000, v4
	v_or_b32_sdwa v75, v5, v2 dst_sel:DWORD dst_unused:UNUSED_PAD src0_sel:DWORD src1_sel:WORD_1
	v_or_b32_sdwa v74, v4, v2 dst_sel:DWORD dst_unused:UNUSED_PAD src0_sel:DWORD src1_sel:WORD_1
	v_sub_f32_e32 v2, v3, v5
	v_and_b32_e32 v4, 0xffff0000, v2
	s_mov_b32 s6, 0xffff0000
	v_sub_f32_e32 v4, v2, v4
	v_lshrrev_b32_e32 v2, 16, v2
	v_and_or_b32 v76, v4, s6, v2
	v_or_b32_sdwa v77, v3, v5 dst_sel:DWORD dst_unused:UNUSED_PAD src0_sel:WORD_1 src1_sel:DWORD
	s_movk_i32 s6, 0xfc00
	s_mov_b64 s[8:9], -1
	v_mfma_f32_32x32x16_bf16 v[2:17], v[22:25], v[74:77], 0
	s_nop 11
	v_cvt_pk_f16_f32 v2, v2, v3
	v_cvt_pk_f16_f32 v3, v4, v5
	v_pk_max_i16 v2, v2, s6 op_sel_hi:[1,0]
	v_pk_max_i16 v3, v3, s6 op_sel_hi:[1,0]
	s_nop 0
	v_exp_f16_e32 v43, v2
	v_exp_f16_e32 v45, v3
	v_exp_f16_sdwa v43, v2 dst_sel:WORD_1 dst_unused:UNUSED_PRESERVE src0_sel:WORD_1
	v_exp_f16_sdwa v45, v3 dst_sel:WORD_1 dst_unused:UNUSED_PRESERVE src0_sel:WORD_1
	v_cvt_pk_f16_f32 v2, v6, v7
	v_cvt_pk_f16_f32 v3, v8, v9
	v_pk_max_i16 v2, v2, s6 op_sel_hi:[1,0]
	v_pk_max_i16 v3, v3, s6 op_sel_hi:[1,0]
	s_nop 0
	v_exp_f16_e32 v50, v2
	v_exp_f16_e32 v54, v3
	v_exp_f16_sdwa v50, v2 dst_sel:WORD_1 dst_unused:UNUSED_PRESERVE src0_sel:WORD_1
	v_exp_f16_sdwa v54, v3 dst_sel:WORD_1 dst_unused:UNUSED_PRESERVE src0_sel:WORD_1
	v_cvt_pk_f16_f32 v2, v10, v11
	v_cvt_pk_f16_f32 v3, v12, v13
	v_pk_max_i16 v2, v2, s6 op_sel_hi:[1,0]
	v_pk_max_i16 v3, v3, s6 op_sel_hi:[1,0]
	s_nop 0
	v_exp_f16_e32 v58, v2
	v_exp_f16_e32 v61, v3
	v_exp_f16_sdwa v58, v2 dst_sel:WORD_1 dst_unused:UNUSED_PRESERVE src0_sel:WORD_1
	v_exp_f16_sdwa v61, v3 dst_sel:WORD_1 dst_unused:UNUSED_PRESERVE src0_sel:WORD_1
	v_cvt_pk_f16_f32 v2, v14, v15
	v_cvt_pk_f16_f32 v3, v16, v17
	v_pk_max_i16 v2, v2, s6 op_sel_hi:[1,0]
	v_pk_max_i16 v3, v3, s6 op_sel_hi:[1,0]
	s_nop 0
	v_exp_f16_e32 v64, v2
	v_exp_f16_e32 v66, v3
	v_exp_f16_sdwa v64, v2 dst_sel:WORD_1 dst_unused:UNUSED_PRESERVE src0_sel:WORD_1
	v_exp_f16_sdwa v66, v3 dst_sel:WORD_1 dst_unused:UNUSED_PRESERVE src0_sel:WORD_1
	v_mfma_f32_32x32x16_bf16 v[2:17], v[18:21], v[74:77], 0
	s_nop 11
	v_cvt_pk_f16_f32 v2, v2, v3
	v_cvt_pk_f16_f32 v3, v4, v5
	v_pk_max_i16 v2, v2, s6 op_sel_hi:[1,0]
	v_pk_max_i16 v3, v3, s6 op_sel_hi:[1,0]
	s_nop 0
	v_exp_f16_e32 v72, v2
	v_exp_f16_e32 v76, v3
	v_exp_f16_sdwa v72, v2 dst_sel:WORD_1 dst_unused:UNUSED_PRESERVE src0_sel:WORD_1
	v_exp_f16_sdwa v76, v3 dst_sel:WORD_1 dst_unused:UNUSED_PRESERVE src0_sel:WORD_1
	v_cvt_pk_f16_f32 v2, v6, v7
	v_cvt_pk_f16_f32 v3, v8, v9
	v_pk_max_i16 v2, v2, s6 op_sel_hi:[1,0]
	v_pk_max_i16 v3, v3, s6 op_sel_hi:[1,0]
	s_nop 0
	v_exp_f16_e32 v83, v2
	v_exp_f16_e32 v85, v3
	v_exp_f16_sdwa v83, v2 dst_sel:WORD_1 dst_unused:UNUSED_PRESERVE src0_sel:WORD_1
	v_exp_f16_sdwa v85, v3 dst_sel:WORD_1 dst_unused:UNUSED_PRESERVE src0_sel:WORD_1
	v_cvt_pk_f16_f32 v2, v10, v11
	v_cvt_pk_f16_f32 v3, v12, v13
	v_pk_max_i16 v2, v2, s6 op_sel_hi:[1,0]
	v_pk_max_i16 v3, v3, s6 op_sel_hi:[1,0]
	s_nop 0
	v_exp_f16_e32 v89, v2
	v_exp_f16_e32 v92, v3
	v_exp_f16_sdwa v89, v2 dst_sel:WORD_1 dst_unused:UNUSED_PRESERVE src0_sel:WORD_1
	v_exp_f16_sdwa v92, v3 dst_sel:WORD_1 dst_unused:UNUSED_PRESERVE src0_sel:WORD_1
	v_cvt_pk_f16_f32 v2, v14, v15
	v_cvt_pk_f16_f32 v3, v16, v17
	v_pk_max_i16 v2, v2, s6 op_sel_hi:[1,0]
	v_pk_max_i16 v3, v3, s6 op_sel_hi:[1,0]
	s_nop 0
	v_exp_f16_e32 v95, v2
	v_exp_f16_e32 v96, v3
	v_exp_f16_sdwa v95, v2 dst_sel:WORD_1 dst_unused:UNUSED_PRESERVE src0_sel:WORD_1
	v_exp_f16_sdwa v96, v3 dst_sel:WORD_1 dst_unused:UNUSED_PRESERVE src0_sel:WORD_1
	s_and_b64 vcc, exec, s[4:5]
	s_cbranch_vccnz .LBB3_16
	s_branch .LBB3_17

.LBB3_166:
	v_cvt_pk_f16_f32 v6, v6, v6
	v_pk_fma_f16 v23, v26, v6, v7
	v_pk_fma_f16 v24, v27, v6, v8
	v_pk_fma_f16 v25, v28, v6, v9
	v_pk_fma_f16 v128, v30, v6, v10
	v_pk_fma_f16 v129, v31, v6, v11
	v_pk_fma_f16 v130, v32, v6, v12
	v_pk_fma_f16 v131, v39, v6, v13
	v_pk_fma_f16 v132, v40, v6, v14
	v_pk_fma_f16 v133, v41, v6, v15
	v_pk_fma_f16 v134, v42, v6, v16
	v_pk_fma_f16 v135, v44, v6, v18
	v_pk_fma_f16 v136, v47, v6, v19
	v_pk_fma_f16 v137, v51, v6, v20
	v_pk_fma_f16 v138, v53, v6, v21
	v_pk_fma_f16 v139, v57, v6, v22
	v_pk_fma_f16 v140, v59, v6, v140
	s_mov_b64 s[4:5], -1
	s_mov_b64 s[6:7], 0
	s_and_b64 vcc, exec, s[4:5]
	s_mov_b64 s[4:5], 0
	s_cbranch_vccz .LBB3_79
	s_branch .LBB3_78
	.p2align	8

	.amdhsa_kernel _Z6k_iterILb0ELb0EEvPKfS1_PKiPK15HIP_vector_typeIfLj4EES7_S1_S1_S3_S1_PfS8_S1_S3_PDF16_PS5_SA_PiSA_SB_
		.amdhsa_group_segment_fixed_size 5808
		.amdhsa_private_segment_fixed_size 0
		.amdhsa_kernarg_size 152
		.amdhsa_user_sgpr_count 2
		.amdhsa_user_sgpr_dispatch_ptr 0
		.amdhsa_user_sgpr_queue_ptr 0
		.amdhsa_user_sgpr_kernarg_segment_ptr 1
		.amdhsa_user_sgpr_dispatch_id 0
		.amdhsa_user_sgpr_kernarg_preload_length 0
		.amdhsa_user_sgpr_kernarg_preload_offset 0
		.amdhsa_user_sgpr_private_segment_size 0
		.amdhsa_uses_dynamic_stack 0
		.amdhsa_enable_private_segment 0
		.amdhsa_system_sgpr_workgroup_id_x 1
		.amdhsa_system_sgpr_workgroup_id_y 0
		.amdhsa_system_sgpr_workgroup_id_z 0
		.amdhsa_system_sgpr_workgroup_info 0
		.amdhsa_system_vgpr_workitem_id 0
		.amdhsa_next_free_vgpr 184
		.amdhsa_next_free_sgpr 36
		.amdhsa_accum_offset 184
		.amdhsa_reserve_vcc 1
		.amdhsa_float_round_mode_32 0
		.amdhsa_float_round_mode_16_64 0
		.amdhsa_float_denorm_mode_32 3
		.amdhsa_float_denorm_mode_16_64 3
		.amdhsa_dx10_clamp 1
		.amdhsa_ieee_mode 1
		.amdhsa_fp16_overflow 0
		.amdhsa_tg_split 0
		.amdhsa_exception_fp_ieee_invalid_op 0
		.amdhsa_exception_fp_denorm_src 0
		.amdhsa_exception_fp_ieee_div_zero 0
		.amdhsa_exception_fp_ieee_overflow 0
		.amdhsa_exception_fp_ieee_underflow 0
		.amdhsa_exception_fp_ieee_inexact 0
		.amdhsa_exception_int_div_zero 0
	.end_amdhsa_kernel

_Z6k_iterILb0ELb1EEvPKfS1_PKiPK15HIP_vector_typeIfLj4EES7_S1_S1_S3_S1_PfS8_S1_S3_PDF16_PS5_SA_PiSA_SB_:
	s_load_dwordx2 s[8:9], s[0:1], 0x80
	s_load_dwordx4 s[4:7], s[0:1], 0x70
	s_load_dwordx4 s[16:19], s[0:1], 0x40
	s_load_dwordx2 s[22:23], s[0:1], 0x50
	v_readfirstlane_b32 s12, v0
	v_cmp_gt_u32_e64 s[14:15], 64, v0
	v_lshlrev_b32_e32 v1, 2, v0
	s_and_saveexec_b64 s[10:11], s[14:15]
	v_mov_b32_e32 v2, 0
	ds_write_b32 v1, v2 offset:5152
	s_or_b64 exec, exec, s[10:11]
	s_lshl_b32 s3, s2, 5
	s_and_b32 s3, s3, 0xe0
	s_lshr_b32 s2, s2, 3
	s_add_i32 s2, s3, s2
	s_lshl_b32 s29, s2, 6
	v_and_b32_e32 v2, 31, v0
	v_or_b32_e32 v4, s29, v2
	v_mov_b32_e32 v5, 0
	s_lshr_b32 s30, s12, 6
	s_lshl_b32 s32, s30, 2
	s_lshr_b32 s32, 0x73261540, s32
	s_lshl_b32 s32, s32, 5
	s_and_b32 s32, s32, 0xe0
	v_or_b32_e32 v176, s32, v2
	v_lshlrev_b32_e32 v177, 4, v176
	v_add_u32_e32 v178, 0x1000, v177
	v_add_u32_e32 v179, 0x2000, v177
	v_add_u32_e32 v180, 0x3000, v177
	v_add_u32_e32 v181, 0x4000, v177
	v_add_u32_e32 v182, 0x5000, v177
	s_mov_b32 s3, 0
	s_lshl_b64 s[34:35], s[2:3], 16
	s_lshl_b32 s33, s2, 2
	s_waitcnt lgkmcnt(0)
	s_load_dword s26, s[8:9], s33 offset:0x0
	s_add_u32 s20, s4, s34
	s_addc_u32 s21, s5, s35
	v_lshl_add_u64 v[4:5], v[4:5], 4, s[6:7]
	global_load_dwordx3 v[30:32], v[4:5], off
	global_load_dwordx3 v[26:28], v[4:5], off offset:512
	global_load_dwordx4 v[2:5], v177, s[20:21]
	global_load_dwordx4 v[6:9], v178, s[20:21]
	global_load_dwordx4 v[10:13], v179, s[20:21]
	global_load_dwordx4 v[14:17], v180, s[20:21]
	global_load_dwordx4 v[18:21], v181, s[20:21]
	global_load_dwordx4 v[22:25], v182, s[20:21]
	v_and_b32_e32 v38, 63, v0
	v_mov_b32_e32 v29, 0xff800000
	v_cmp_gt_u32_e64 s[0:1], 32, v38
	s_waitcnt lgkmcnt(0)
	s_cmpk_gt_i32 s26, 0x600
	s_cselect_b64 s[24:25], -1, 0
	s_cmpk_lt_i32 s26, 0x601
	s_cbranch_scc1 .LBB4_6
	s_and_saveexec_b64 s[8:9], s[14:15]
	s_cbranch_execz .LBB4_5
	v_or_b32_e32 v178, s29, v0
	v_mov_b32_e32 v179, 0
	v_lshl_add_u64 v[178:179], v[178:179], 4, s[6:7]
	global_load_dwordx4 v[178:181], v[178:179], off
	v_lshlrev_b32_e32 v177, 4, v0
	s_waitcnt vmcnt(0)
	ds_write_b128 v177, v[178:181] offset:2080

.LBB4_6:
	s_xor_b32 s33, s32, 0xff
	s_add_i32 s33, s33, s26
	s_ashr_i32 s27, s33, 8
	v_cmp_gt_i32_e32 vcc, s26, v176
	v_med3_i32 v33, s27, 0, 6
	s_sub_i32 s33, s26, 0x100
	v_cmp_gt_i32_e64 s[4:5], s33, v176
	s_sub_i32 s33, s26, 0x200
	v_cmp_gt_i32_e64 s[6:7], s33, v176
	s_sub_i32 s33, s26, 0x300
	v_cmp_gt_i32_e64 s[8:9], s33, v176
	s_sub_i32 s33, s26, 0x400
	v_cmp_gt_i32_e64 s[10:11], s33, v176
	s_sub_i32 s33, s26, 0x500
	v_cmp_gt_i32_e64 s[12:13], s33, v176
	s_and_b32 s27, s29, 0x7ffff000
	s_mov_b32 s2, 0xffff0000
	v_readfirstlane_b32 s28, v33
	s_nop 3
	s_cmp_lt_i32 s28, 4
	s_waitcnt vmcnt(5)
	v_cndmask_b32_e32 v4, v29, v4, vcc
	v_cndmask_b32_e64 v134, v3, v2, s[0:1]
	v_cndmask_b32_e32 v134, 0, v134, vcc
	s_waitcnt vmcnt(4)
	v_cndmask_b32_e64 v3, v29, v8, s[4:5]
	v_cndmask_b32_e64 v97, v7, v6, s[0:1]
	v_cndmask_b32_e64 v97, 0, v97, s[4:5]
	v_cndmask_b32_e64 v135, 1.0, v4, s[0:1]
	v_cndmask_b32_e64 v33, -1, v9, s[4:5]
	v_cndmask_b32_e64 v98, 1.0, v3, s[0:1]
	s_waitcnt vmcnt(3)
	v_cndmask_b32_e64 v6, v29, v12, s[6:7]
	v_cndmask_b32_e64 v68, v11, v10, s[0:1]
	v_cndmask_b32_e64 v68, 0, v68, s[6:7]
	s_waitcnt vmcnt(2)
	v_cndmask_b32_e64 v7, v29, v16, s[8:9]
	v_cndmask_b32_e64 v70, 1.0, v6, s[0:1]
	v_cndmask_b32_e64 v73, 1.0, v7, s[0:1]
	v_cndmask_b32_e64 v34, -1, v13, s[6:7]
	v_cndmask_b32_e64 v35, -1, v17, s[8:9]
	v_cndmask_b32_e64 v71, v15, v14, s[0:1]
	v_cndmask_b32_e64 v71, 0, v71, s[8:9]
	s_waitcnt vmcnt(1)
	v_cndmask_b32_e64 v8, v29, v20, s[10:11]
	v_cndmask_b32_e64 v48, 1.0, v8, s[0:1]
	s_waitcnt vmcnt(0)
	v_cndmask_b32_e64 v10, v29, v24, s[12:13]
	v_cndmask_b32_e32 v29, -1, v5, vcc
	v_max_i32_e32 v4, 0, v29
	v_add_u32_e32 v4, s27, v4
	v_mov_b32_e32 v5, 0
	v_lshl_add_u64 v[6:7], v[4:5], 2, s[16:17]
	v_max_i32_e32 v4, 0, v33
	v_add_u32_e32 v4, s27, v4
	v_lshl_add_u64 v[8:9], v[4:5], 2, s[16:17]
	v_max_i32_e32 v4, 0, v34
	v_add_u32_e32 v4, s27, v4
	v_cndmask_b32_e64 v3, 1.0, v10, s[0:1]
	v_lshl_add_u64 v[10:11], v[4:5], 2, s[16:17]
	v_max_i32_e32 v4, 0, v35
	v_cndmask_b32_e64 v36, -1, v21, s[10:11]
	v_add_u32_e32 v4, s27, v4
	v_lshl_add_u64 v[12:13], v[4:5], 2, s[16:17]
	v_max_i32_e32 v4, 0, v36
	v_cndmask_b32_e64 v37, -1, v25, s[12:13]
	v_add_u32_e32 v4, s27, v4
	v_lshl_add_u64 v[14:15], v[4:5], 2, s[16:17]
	v_max_i32_e32 v4, 0, v37
	v_cndmask_b32_e64 v46, v19, v18, s[0:1]
	v_cndmask_b32_e64 v46, 0, v46, s[10:11]
	v_cndmask_b32_e64 v2, v23, v22, s[0:1]
	v_cndmask_b32_e64 v2, 0, v2, s[12:13]
	v_add_u32_e32 v4, s27, v4
	v_lshl_add_u64 v[4:5], v[4:5], 2, s[16:17]
	global_load_dword v133, v[6:7], off
	global_load_dword v132, v[8:9], off
	global_load_dword v131, v[10:11], off
	global_load_dword v130, v[12:13], off
	global_load_dword v129, v[14:15], off
	global_load_dword v128, v[4:5], off
	v_max_f32_e32 v6, v32, v32
	v_cndmask_b32_e64 v4, v31, v30, s[0:1]
	v_max_f32_e32 v6, 0xc6ea6000, v6
	v_cndmask_b32_e64 v6, v6, 1.0, s[0:1]
	v_and_b32_e32 v7, 0xffff0000, v4
	v_sub_f32_e32 v8, v4, v7
	v_or_b32_sdwa v22, v4, v7 dst_sel:DWORD dst_unused:UNUSED_PAD src0_sel:WORD_1 src1_sel:DWORD
	v_and_b32_e32 v4, 0xffff0000, v6
	v_sub_f32_e32 v7, v6, v4
	v_or_b32_sdwa v24, v6, v4 dst_sel:DWORD dst_unused:UNUSED_PAD src0_sel:WORD_1 src1_sel:DWORD
	v_or_b32_sdwa v23, v8, v4 dst_sel:DWORD dst_unused:UNUSED_PAD src0_sel:WORD_1 src1_sel:DWORD
	v_max_f32_e32 v4, v28, v28
	v_cndmask_b32_e64 v5, v27, v26, s[0:1]
	v_and_b32_e32 v9, 0xffff0000, v7
	v_max_f32_e32 v4, 0xc6ea6000, v4
	v_sub_f32_e32 v9, v7, v9
	v_lshrrev_b32_e32 v7, 16, v7
	v_cndmask_b32_e64 v4, v4, 1.0, s[0:1]
	v_and_b32_e32 v6, 0xffff0000, v5
	v_and_or_b32 v25, v9, s2, v7
	v_sub_f32_e32 v7, v5, v6
	v_or_b32_sdwa v18, v5, v6 dst_sel:DWORD dst_unused:UNUSED_PAD src0_sel:WORD_1 src1_sel:DWORD
	v_and_b32_e32 v5, 0xffff0000, v4
	v_sub_f32_e32 v6, v4, v5
	v_and_b32_e32 v8, 0xffff0000, v6
	v_sub_f32_e32 v8, v6, v8
	v_lshrrev_b32_e32 v6, 16, v6
	v_or_b32_sdwa v20, v4, v5 dst_sel:DWORD dst_unused:UNUSED_PAD src0_sel:WORD_1 src1_sel:DWORD
	v_or_b32_sdwa v19, v7, v5 dst_sel:DWORD dst_unused:UNUSED_PAD src0_sel:WORD_1 src1_sel:DWORD
	v_and_or_b32 v21, v8, s2, v6
	s_mov_b64 s[2:3], 0
	s_cbranch_scc1 .LBB4_11
	s_cmp_gt_i32 s28, 4
	s_cbranch_scc0 .LBB4_14
	s_cmp_gt_i32 s28, 5
	s_cbranch_scc0 .LBB4_15
	s_cmp_eq_u32 s28, 6
	s_mov_b64 s[4:5], 0
	s_cbranch_scc0 .LBB4_48
	v_and_b32_e32 v4, 0xffff0000, v2
	v_max_f32_e32 v3, v3, v3
	v_sub_f32_e32 v4, v2, v4
	v_max_f32_e32 v3, 0xc6ea6000, v3
	v_and_b32_e32 v5, 0xffff0000, v3
	v_and_b32_e32 v4, 0xffff0000, v4
	v_or_b32_sdwa v75, v5, v2 dst_sel:DWORD dst_unused:UNUSED_PAD src0_sel:DWORD src1_sel:WORD_1
	v_or_b32_sdwa v74, v4, v2 dst_sel:DWORD dst_unused:UNUSED_PAD src0_sel:DWORD src1_sel:WORD_1
	v_sub_f32_e32 v2, v3, v5
	v_and_b32_e32 v4, 0xffff0000, v2
	s_mov_b32 s6, 0xffff0000
	v_sub_f32_e32 v4, v2, v4
	v_lshrrev_b32_e32 v2, 16, v2
	v_and_or_b32 v76, v4, s6, v2
	v_or_b32_sdwa v77, v3, v5 dst_sel:DWORD dst_unused:UNUSED_PAD src0_sel:WORD_1 src1_sel:DWORD
	s_movk_i32 s6, 0xfc00
	s_mov_b64 s[8:9], -1
	v_mfma_f32_32x32x16_bf16 v[2:17], v[22:25], v[74:77], 0
	s_nop 11
	v_cvt_pk_f16_f32 v2, v2, v3
	v_cvt_pk_f16_f32 v3, v4, v5
	v_pk_max_i16 v2, v2, s6 op_sel_hi:[1,0]
	v_pk_max_i16 v3, v3, s6 op_sel_hi:[1,0]
	s_nop 0
	v_exp_f16_e32 v43, v2
	v_exp_f16_e32 v45, v3
	v_exp_f16_sdwa v43, v2 dst_sel:WORD_1 dst_unused:UNUSED_PRESERVE src0_sel:WORD_1
	v_exp_f16_sdwa v45, v3 dst_sel:WORD_1 dst_unused:UNUSED_PRESERVE src0_sel:WORD_1
	v_cvt_pk_f16_f32 v2, v6, v7
	v_cvt_pk_f16_f32 v3, v8, v9
	v_pk_max_i16 v2, v2, s6 op_sel_hi:[1,0]
	v_pk_max_i16 v3, v3, s6 op_sel_hi:[1,0]
	s_nop 0
	v_exp_f16_e32 v50, v2
	v_exp_f16_e32 v54, v3
	v_exp_f16_sdwa v50, v2 dst_sel:WORD_1 dst_unused:UNUSED_PRESERVE src0_sel:WORD_1
	v_exp_f16_sdwa v54, v3 dst_sel:WORD_1 dst_unused:UNUSED_PRESERVE src0_sel:WORD_1
	v_cvt_pk_f16_f32 v2, v10, v11
	v_cvt_pk_f16_f32 v3, v12, v13
	v_pk_max_i16 v2, v2, s6 op_sel_hi:[1,0]
	v_pk_max_i16 v3, v3, s6 op_sel_hi:[1,0]
	s_nop 0
	v_exp_f16_e32 v58, v2
	v_exp_f16_e32 v61, v3
	v_exp_f16_sdwa v58, v2 dst_sel:WORD_1 dst_unused:UNUSED_PRESERVE src0_sel:WORD_1
	v_exp_f16_sdwa v61, v3 dst_sel:WORD_1 dst_unused:UNUSED_PRESERVE src0_sel:WORD_1
	v_cvt_pk_f16_f32 v2, v14, v15
	v_cvt_pk_f16_f32 v3, v16, v17
	v_pk_max_i16 v2, v2, s6 op_sel_hi:[1,0]
	v_pk_max_i16 v3, v3, s6 op_sel_hi:[1,0]
	s_nop 0
	v_exp_f16_e32 v64, v2
	v_exp_f16_e32 v66, v3
	v_exp_f16_sdwa v64, v2 dst_sel:WORD_1 dst_unused:UNUSED_PRESERVE src0_sel:WORD_1
	v_exp_f16_sdwa v66, v3 dst_sel:WORD_1 dst_unused:UNUSED_PRESERVE src0_sel:WORD_1
	v_mfma_f32_32x32x16_bf16 v[2:17], v[18:21], v[74:77], 0
	s_nop 11
	v_cvt_pk_f16_f32 v2, v2, v3
	v_cvt_pk_f16_f32 v3, v4, v5
	v_pk_max_i16 v2, v2, s6 op_sel_hi:[1,0]
	v_pk_max_i16 v3, v3, s6 op_sel_hi:[1,0]
	s_nop 0
	v_exp_f16_e32 v72, v2
	v_exp_f16_e32 v76, v3
	v_exp_f16_sdwa v72, v2 dst_sel:WORD_1 dst_unused:UNUSED_PRESERVE src0_sel:WORD_1
	v_exp_f16_sdwa v76, v3 dst_sel:WORD_1 dst_unused:UNUSED_PRESERVE src0_sel:WORD_1
	v_cvt_pk_f16_f32 v2, v6, v7
	v_cvt_pk_f16_f32 v3, v8, v9
	v_pk_max_i16 v2, v2, s6 op_sel_hi:[1,0]
	v_pk_max_i16 v3, v3, s6 op_sel_hi:[1,0]
	s_nop 0
	v_exp_f16_e32 v83, v2
	v_exp_f16_e32 v85, v3
	v_exp_f16_sdwa v83, v2 dst_sel:WORD_1 dst_unused:UNUSED_PRESERVE src0_sel:WORD_1
	v_exp_f16_sdwa v85, v3 dst_sel:WORD_1 dst_unused:UNUSED_PRESERVE src0_sel:WORD_1
	v_cvt_pk_f16_f32 v2, v10, v11
	v_cvt_pk_f16_f32 v3, v12, v13
	v_pk_max_i16 v2, v2, s6 op_sel_hi:[1,0]
	v_pk_max_i16 v3, v3, s6 op_sel_hi:[1,0]
	s_nop 0
	v_exp_f16_e32 v89, v2
	v_exp_f16_e32 v92, v3
	v_exp_f16_sdwa v89, v2 dst_sel:WORD_1 dst_unused:UNUSED_PRESERVE src0_sel:WORD_1
	v_exp_f16_sdwa v92, v3 dst_sel:WORD_1 dst_unused:UNUSED_PRESERVE src0_sel:WORD_1
	v_cvt_pk_f16_f32 v2, v14, v15
	v_cvt_pk_f16_f32 v3, v16, v17
	v_pk_max_i16 v2, v2, s6 op_sel_hi:[1,0]
	v_pk_max_i16 v3, v3, s6 op_sel_hi:[1,0]
	s_nop 0
	v_exp_f16_e32 v95, v2
	v_exp_f16_e32 v96, v3
	v_exp_f16_sdwa v95, v2 dst_sel:WORD_1 dst_unused:UNUSED_PRESERVE src0_sel:WORD_1
	v_exp_f16_sdwa v96, v3 dst_sel:WORD_1 dst_unused:UNUSED_PRESERVE src0_sel:WORD_1
	s_and_b64 vcc, exec, s[4:5]
	s_cbranch_vccnz .LBB4_16
	s_branch .LBB4_17

	.amdhsa_kernel _Z6k_iterILb0ELb1EEvPKfS1_PKiPK15HIP_vector_typeIfLj4EES7_S1_S1_S3_S1_PfS8_S1_S3_PDF16_PS5_SA_PiSA_SB_
		.amdhsa_group_segment_fixed_size 5808
		.amdhsa_private_segment_fixed_size 0
		.amdhsa_kernarg_size 152
		.amdhsa_user_sgpr_count 2
		.amdhsa_user_sgpr_dispatch_ptr 0
		.amdhsa_user_sgpr_queue_ptr 0
		.amdhsa_user_sgpr_kernarg_segment_ptr 1
		.amdhsa_user_sgpr_dispatch_id 0
		.amdhsa_user_sgpr_kernarg_preload_length 0
		.amdhsa_user_sgpr_kernarg_preload_offset 0
		.amdhsa_user_sgpr_private_segment_size 0
		.amdhsa_uses_dynamic_stack 0
		.amdhsa_enable_private_segment 0
		.amdhsa_system_sgpr_workgroup_id_x 1
		.amdhsa_system_sgpr_workgroup_id_y 0
		.amdhsa_system_sgpr_workgroup_id_z 0
		.amdhsa_system_sgpr_workgroup_info 0
		.amdhsa_system_vgpr_workitem_id 0
		.amdhsa_next_free_vgpr 184
		.amdhsa_next_free_sgpr 36
		.amdhsa_accum_offset 184
		.amdhsa_reserve_vcc 1
		.amdhsa_float_round_mode_32 0
		.amdhsa_float_round_mode_16_64 0
		.amdhsa_float_denorm_mode_32 3
		.amdhsa_float_denorm_mode_16_64 3
		.amdhsa_dx10_clamp 1
		.amdhsa_ieee_mode 1
		.amdhsa_fp16_overflow 0
		.amdhsa_tg_split 0
		.amdhsa_exception_fp_ieee_invalid_op 0
		.amdhsa_exception_fp_denorm_src 0
		.amdhsa_exception_fp_ieee_div_zero 0
		.amdhsa_exception_fp_ieee_overflow 0
		.amdhsa_exception_fp_ieee_underflow 0
		.amdhsa_exception_fp_ieee_inexact 0
		.amdhsa_exception_int_div_zero 0
	.end_amdhsa_kernel

	.text
	.p2alignl 8, 3212836864
	.fill 256, 4, 3212836864

amdhsa.kernels:
  - .agpr_count:     0
    .args:
      - .actual_access:  read_only
        .address_space:  global
        .offset:         0
        .size:           8
        .value_kind:     global_buffer
      - .actual_access:  read_only
        .address_space:  global
        .offset:         8
        .size:           8
        .value_kind:     global_buffer
      - .actual_access:  read_only
        .address_space:  global
        .offset:         16
        .size:           8
        .value_kind:     global_buffer
      - .actual_access:  read_only
        .address_space:  global
        .offset:         24
        .size:           8
        .value_kind:     global_buffer
      - .actual_access:  write_only
        .address_space:  global
        .offset:         32
        .size:           8
        .value_kind:     global_buffer
      - .actual_access:  write_only
        .address_space:  global
        .offset:         40
        .size:           8
        .value_kind:     global_buffer
      - .actual_access:  write_only
        .address_space:  global
        .offset:         48
        .size:           8
        .value_kind:     global_buffer
      - .actual_access:  write_only
        .address_space:  global
        .offset:         56
        .size:           8
        .value_kind:     global_buffer
      - .actual_access:  write_only
        .address_space:  global
        .offset:         64
        .size:           8
        .value_kind:     global_buffer
      - .actual_access:  write_only
        .address_space:  global
        .offset:         72
        .size:           8
        .value_kind:     global_buffer
      - .actual_access:  write_only
        .address_space:  global
        .offset:         80
        .size:           8
        .value_kind:     global_buffer
      - .actual_access:  write_only
        .address_space:  global
        .offset:         88
        .size:           8
        .value_kind:     global_buffer
      - .actual_access:  write_only
        .address_space:  global
        .offset:         96
        .size:           8
        .value_kind:     global_buffer
      - .actual_access:  write_only
        .address_space:  global
        .offset:         104
        .size:           8
        .value_kind:     global_buffer
      - .actual_access:  write_only
        .address_space:  global
        .offset:         112
        .size:           8
        .value_kind:     global_buffer
    .group_segment_fixed_size: 67584
    .kernarg_segment_align: 8
    .kernarg_segment_size: 120
    .language:       OpenCL C
    .language_version:
      - 2
      - 0
    .max_flat_workgroup_size: 1024
    .name:           _Z6k_sortPKfS0_PKiS2_PiP15HIP_vector_typeIfLj4EEPfS7_S3_S7_S7_S3_S3_S6_S6_
    .private_segment_fixed_size: 0
    .sgpr_count:     35
    .sgpr_spill_count: 0
    .symbol:         _Z6k_sortPKfS0_PKiS2_PiP15HIP_vector_typeIfLj4EEPfS7_S3_S7_S7_S3_S3_S6_S6_.kd
    .uniform_work_group_size: 1
    .uses_dynamic_stack: false
    .vgpr_count:     40
    .vgpr_spill_count: 0
    .wavefront_size: 64
  - .agpr_count:     0
    .args:
      - .actual_access:  read_only
        .address_space:  global
        .offset:         0
        .size:           8
        .value_kind:     global_buffer
      - .actual_access:  read_only
        .address_space:  global
        .offset:         8
        .size:           8
        .value_kind:     global_buffer
      - .actual_access:  read_only
        .address_space:  global
        .offset:         16
        .size:           8
        .value_kind:     global_buffer
      - .actual_access:  read_only
        .address_space:  global
        .offset:         24
        .size:           8
        .value_kind:     global_buffer
      - .actual_access:  read_only
        .address_space:  global
        .offset:         32
        .size:           8
        .value_kind:     global_buffer
      - .actual_access:  read_only
        .address_space:  global
        .offset:         40
        .size:           8
        .value_kind:     global_buffer
      - .actual_access:  read_only
        .address_space:  global
        .offset:         48
        .size:           8
        .value_kind:     global_buffer
      - .actual_access:  write_only
        .address_space:  global
        .offset:         56
        .size:           8
        .value_kind:     global_buffer
    .group_segment_fixed_size: 145952
    .kernarg_segment_align: 8
    .kernarg_segment_size: 64
    .language:       OpenCL C
    .language_version:
      - 2
      - 0
    .max_flat_workgroup_size: 512
    .name:           _Z7k_finalPK15HIP_vector_typeIfLj4EES2_PKiS4_PKfS6_PKDF16_Pf
    .private_segment_fixed_size: 0
    .sgpr_count:     34
    .sgpr_spill_count: 0
    .symbol:         _Z7k_finalPK15HIP_vector_typeIfLj4EES2_PKiS4_PKfS6_PKDF16_Pf.kd
    .uniform_work_group_size: 1
    .uses_dynamic_stack: false
    .vgpr_count:     177
    .vgpr_spill_count: 0
    .wavefront_size: 64
  - .agpr_count:     0
    .args:
      - .actual_access:  read_only
        .address_space:  global
        .offset:         0
        .size:           8
        .value_kind:     global_buffer
      - .actual_access:  read_only
        .address_space:  global
        .offset:         8
        .size:           8
        .value_kind:     global_buffer
      - .actual_access:  read_only
        .address_space:  global
        .offset:         16
        .size:           8
        .value_kind:     global_buffer
      - .actual_access:  read_only
        .address_space:  global
        .offset:         24
        .size:           8
        .value_kind:     global_buffer
      - .actual_access:  read_only
        .address_space:  global
        .offset:         32
        .size:           8
        .value_kind:     global_buffer
      - .actual_access:  read_only
        .address_space:  global
        .offset:         40
        .size:           8
        .value_kind:     global_buffer
      - .actual_access:  read_only
        .address_space:  global
        .offset:         48
        .size:           8
        .value_kind:     global_buffer
      - .actual_access:  read_only
        .address_space:  global
        .offset:         56
        .size:           8
        .value_kind:     global_buffer
      - .actual_access:  read_only
        .address_space:  global
        .offset:         64
        .size:           8
        .value_kind:     global_buffer
      - .address_space:  global
        .offset:         72
        .size:           8
        .value_kind:     global_buffer
      - .actual_access:  read_only
        .address_space:  global
        .offset:         80
        .size:           8
        .value_kind:     global_buffer
      - .actual_access:  read_only
        .address_space:  global
        .offset:         88
        .size:           8
        .value_kind:     global_buffer
      - .actual_access:  read_only
        .address_space:  global
        .offset:         96
        .size:           8
        .value_kind:     global_buffer
      - .actual_access:  write_only
        .address_space:  global
        .offset:         104
        .size:           8
        .value_kind:     global_buffer
      - .address_space:  global
        .offset:         112
        .size:           8
        .value_kind:     global_buffer
      - .actual_access:  write_only
        .address_space:  global
        .offset:         120
        .size:           8
        .value_kind:     global_buffer
      - .actual_access:  write_only
        .address_space:  global
        .offset:         128
        .size:           8
        .value_kind:     global_buffer
      - .actual_access:  write_only
        .address_space:  global
        .offset:         136
        .size:           8
        .value_kind:     global_buffer
      - .actual_access:  write_only
        .address_space:  global
        .offset:         144
        .size:           8
        .value_kind:     global_buffer
    .group_segment_fixed_size: 30384
    .kernarg_segment_align: 8
    .kernarg_segment_size: 152
    .language:       OpenCL C
    .language_version:
      - 2
      - 0
    .max_flat_workgroup_size: 512
    .name:           _Z6k_iterILb1ELb0EEvPKfS1_PKiPK15HIP_vector_typeIfLj4EES7_S1_S1_S3_S1_PfS8_S1_S3_PDF16_PS5_SA_PiSA_SB_
    .private_segment_fixed_size: 0
    .sgpr_count:     71
    .sgpr_spill_count: 0
    .symbol:         _Z6k_iterILb1ELb0EEvPKfS1_PKiPK15HIP_vector_typeIfLj4EES7_S1_S1_S3_S1_PfS8_S1_S3_PDF16_PS5_SA_PiSA_SB_.kd
    .uniform_work_group_size: 1
    .uses_dynamic_stack: false
    .vgpr_count:     142
    .vgpr_spill_count: 0
    .wavefront_size: 64
  - .agpr_count:     0
    .args:
      - .actual_access:  read_only
        .address_space:  global
        .offset:         0
        .size:           8
        .value_kind:     global_buffer
      - .actual_access:  read_only
        .address_space:  global
        .offset:         8
        .size:           8
        .value_kind:     global_buffer
      - .actual_access:  read_only
        .address_space:  global
        .offset:         16
        .size:           8
        .value_kind:     global_buffer
      - .actual_access:  read_only
        .address_space:  global
        .offset:         24
        .size:           8
        .value_kind:     global_buffer
      - .actual_access:  read_only
        .address_space:  global
        .offset:         32
        .size:           8
        .value_kind:     global_buffer
      - .actual_access:  read_only
        .address_space:  global
        .offset:         40
        .size:           8
        .value_kind:     global_buffer
      - .actual_access:  read_only
        .address_space:  global
        .offset:         48
        .size:           8
        .value_kind:     global_buffer
      - .actual_access:  read_only
        .address_space:  global
        .offset:         56
        .size:           8
        .value_kind:     global_buffer
      - .actual_access:  read_only
        .address_space:  global
        .offset:         64
        .size:           8
        .value_kind:     global_buffer
      - .address_space:  global
        .offset:         72
        .size:           8
        .value_kind:     global_buffer
      - .actual_access:  read_only
        .address_space:  global
        .offset:         80
        .size:           8
        .value_kind:     global_buffer
      - .actual_access:  read_only
        .address_space:  global
        .offset:         88
        .size:           8
        .value_kind:     global_buffer
      - .actual_access:  read_only
        .address_space:  global
        .offset:         96
        .size:           8
        .value_kind:     global_buffer
      - .actual_access:  read_only
        .address_space:  global
        .offset:         104
        .size:           8
        .value_kind:     global_buffer
      - .actual_access:  read_only
        .address_space:  global
        .offset:         112
        .size:           8
        .value_kind:     global_buffer
      - .actual_access:  read_only
        .address_space:  global
        .offset:         120
        .size:           8
        .value_kind:     global_buffer
      - .actual_access:  read_only
        .address_space:  global
        .offset:         128
        .size:           8
        .value_kind:     global_buffer
      - .actual_access:  read_only
        .address_space:  global
        .offset:         136
        .size:           8
        .value_kind:     global_buffer
      - .actual_access:  read_only
        .address_space:  global
        .offset:         144
        .size:           8
        .value_kind:     global_buffer
    .group_segment_fixed_size: 5808
    .kernarg_segment_align: 8
    .kernarg_segment_size: 152
    .language:       OpenCL C
    .language_version:
      - 2
      - 0
    .max_flat_workgroup_size: 512
    .name:           _Z6k_iterILb0ELb0EEvPKfS1_PKiPK15HIP_vector_typeIfLj4EES7_S1_S1_S3_S1_PfS8_S1_S3_PDF16_PS5_SA_PiSA_SB_
    .private_segment_fixed_size: 0
    .sgpr_count:     42
    .sgpr_spill_count: 0
    .symbol:         _Z6k_iterILb0ELb0EEvPKfS1_PKiPK15HIP_vector_typeIfLj4EES7_S1_S1_S3_S1_PfS8_S1_S3_PDF16_PS5_SA_PiSA_SB_.kd
    .uniform_work_group_size: 1
    .uses_dynamic_stack: false
    .vgpr_count:     184
    .vgpr_spill_count: 0
    .wavefront_size: 64
  - .agpr_count:     0
    .args:
      - .actual_access:  read_only
        .address_space:  global
        .offset:         0
        .size:           8
        .value_kind:     global_buffer
      - .actual_access:  read_only
        .address_space:  global
        .offset:         8
        .size:           8
        .value_kind:     global_buffer
      - .actual_access:  read_only
        .address_space:  global
        .offset:         16
        .size:           8
        .value_kind:     global_buffer
      - .actual_access:  read_only
        .address_space:  global
        .offset:         24
        .size:           8
        .value_kind:     global_buffer
      - .actual_access:  read_only
        .address_space:  global
        .offset:         32
        .size:           8
        .value_kind:     global_buffer
      - .actual_access:  read_only
        .address_space:  global
        .offset:         40
        .size:           8
        .value_kind:     global_buffer
      - .actual_access:  read_only
        .address_space:  global
        .offset:         48
        .size:           8
        .value_kind:     global_buffer
      - .actual_access:  read_only
        .address_space:  global
        .offset:         56
        .size:           8
        .value_kind:     global_buffer
      - .actual_access:  read_only
        .address_space:  global
        .offset:         64
        .size:           8
        .value_kind:     global_buffer
      - .address_space:  global
        .offset:         72
        .size:           8
        .value_kind:     global_buffer
      - .actual_access:  write_only
        .address_space:  global
        .offset:         80
        .size:           8
        .value_kind:     global_buffer
      - .actual_access:  read_only
        .address_space:  global
        .offset:         88
        .size:           8
        .value_kind:     global_buffer
      - .actual_access:  read_only
        .address_space:  global
        .offset:         96
        .size:           8
        .value_kind:     global_buffer
      - .actual_access:  read_only
        .address_space:  global
        .offset:         104
        .size:           8
        .value_kind:     global_buffer
      - .actual_access:  read_only
        .address_space:  global
        .offset:         112
        .size:           8
        .value_kind:     global_buffer
      - .actual_access:  read_only
        .address_space:  global
        .offset:         120
        .size:           8
        .value_kind:     global_buffer
      - .actual_access:  read_only
        .address_space:  global
        .offset:         128
        .size:           8
        .value_kind:     global_buffer
      - .actual_access:  read_only
        .address_space:  global
        .offset:         136
        .size:           8
        .value_kind:     global_buffer
      - .actual_access:  read_only
        .address_space:  global
        .offset:         144
        .size:           8
        .value_kind:     global_buffer
    .group_segment_fixed_size: 5808
    .kernarg_segment_align: 8
    .kernarg_segment_size: 152
    .language:       OpenCL C
    .language_version:
      - 2
      - 0
    .max_flat_workgroup_size: 512
    .name:           _Z6k_iterILb0ELb1EEvPKfS1_PKiPK15HIP_vector_typeIfLj4EES7_S1_S1_S3_S1_PfS8_S1_S3_PDF16_PS5_SA_PiSA_SB_
    .private_segment_fixed_size: 0
    .sgpr_count:     42
    .sgpr_spill_count: 0
    .symbol:         _Z6k_iterILb0ELb1EEvPKfS1_PKiPK15HIP_vector_typeIfLj4EES7_S1_S1_S3_S1_PfS8_S1_S3_PDF16_PS5_SA_PiSA_SB_.kd
    .uniform_work_group_size: 1
    .uses_dynamic_stack: false
    .vgpr_count:     184
    .vgpr_spill_count: 0
    .wavefront_size: 64
